# v79 with the P6 start stagger removed (all workgroup groups start their first unit together)
# speedup vs baseline: 1.0108x; 1.0108x over previous
.LBB0_764:
	s_or_b64 exec, exec, s[0:1]
	s_mov_b32 s0, 0
	s_cmp_eq_u32 s0, 0
	v_readfirstlane_b32 s21, v2
	s_waitcnt lgkmcnt(0)
	s_barrier
	s_cbranch_scc1 .LBB0_766
